# K3 gather: both loads in flight + kernarg/usage loads hoisted; K2 kernarg loads hoisted
# speedup vs baseline: 1.0222x; 1.0222x over previous
_Z9k2_reducePKfS0_S0_PdPiS1_:
	s_load_dwordx4 s[12:15], s[0:1], 0x0
	s_load_dwordx2 s[4:5], s[0:1], 0x10
	s_load_dwordx4 s[28:31], s[0:1], 0x18
	s_load_dwordx2 s[32:33], s[0:1], 0x28
	v_lshrrev_b32_e32 v1, 3, v0
	s_lshr_b32 s3, s2, 3
	s_lshr_b32 s7, s2, 7
	v_and_b32_e32 v2, 14, v1
	v_add_lshl_u32 v34, v2, s7, 6
	s_lshl_b32 s7, s3, 2
	s_and_b32 s6, s2, 7
	s_and_b32 s16, s7, 48
	s_waitcnt lgkmcnt(0)
	s_and_b32 s9, s15, 0xffff
	s_mov_b32 s8, s14
	s_mul_hi_u32 s14, s3, 0x1f400
	s_mul_i32 s3, s3, 0x1f400
	s_add_u32 s3, s12, s3
	s_addc_u32 s13, s13, s14
	s_mul_i32 s12, s6, 0x3e80
	s_add_u32 s12, s3, s12
	s_addc_u32 s3, s13, 0
	s_mov_b32 s11, 0x20000
	s_and_b32 s13, s3, 0xffff
	s_lshl_b32 s3, s6, 14
	s_and_b32 s7, s7, 12
	s_movk_i32 s14, 0x3e80
	s_mov_b32 s15, s11
	s_or_b32 s17, s7, s3
	s_lshl_b32 s3, s6, 7
	v_lshlrev_b32_e32 v36, 4, v0
	s_movk_i32 s6, 0x800
	buffer_load_dwordx4 v[30:33], v36, s[12:15], 0 offen
	buffer_load_dwordx4 v[26:29], v36, s[12:15], s6 offen
	s_movk_i32 s18, 0x1000
	s_movk_i32 s6, 0x1800
	buffer_load_dwordx4 v[22:25], v36, s[12:15], s18 offen
	buffer_load_dwordx4 v[18:21], v36, s[12:15], s6 offen
	s_movk_i32 s19, 0x2000
	s_movk_i32 s6, 0x2800
	s_movk_i32 s20, 0x3000
	buffer_load_dwordx4 v[14:17], v36, s[12:15], s19 offen
	buffer_load_dwordx4 v[10:13], v36, s[12:15], s6 offen
	s_movk_i32 s6, 0x3800
	buffer_load_dwordx4 v[6:9], v36, s[12:15], s20 offen
	buffer_load_dwordx4 v[2:5], v36, s[12:15], s6 offen
	v_and_b32_e32 v36, 15, v0
	v_or3_b32 v34, v34, s16, v36
	s_mov_b32 s10, 0x400000
	v_or_b32_e32 v35, s3, v0
	v_lshl_add_u32 v34, v34, 4, s17
	s_mov_b32 s12, 0x40000
	s_and_b32 s5, s5, 0xffff
	s_mov_b32 s6, s11
	s_mov_b32 s7, s11
	v_lshlrev_b32_e32 v35, 2, v35
	s_mov_b32 s13, 0x60000
	s_mov_b32 s14, 0x80000
	s_mov_b32 s16, 0xa0000
	s_mov_b32 s21, 0xc0000
	s_mov_b32 s23, 0xe0000
	buffer_load_dword v40, v34, s[8:11], 0 offen
	buffer_load_dword v41, v34, s[8:11], s11 offen
	buffer_load_dword v42, v34, s[8:11], s12 offen
	buffer_load_dword v43, v34, s[8:11], s13 offen
	buffer_load_dword v44, v34, s[8:11], s14 offen
	buffer_load_dword v45, v34, s[8:11], s16 offen
	buffer_load_dword v46, v34, s[8:11], s21 offen
	buffer_load_dword v47, v34, s[8:11], s23 offen
	s_movk_i32 s12, 0x7000
	s_movk_i32 s15, 0x4000
	s_movk_i32 s17, 0x5000
	s_movk_i32 s22, 0x6000
	buffer_load_dword v48, v35, s[4:7], 0 offen
	buffer_load_dword v49, v35, s[4:7], s18 offen
	buffer_load_dword v50, v35, s[4:7], s19 offen
	buffer_load_dword v51, v35, s[4:7], s20 offen
	buffer_load_dword v52, v35, s[4:7], s15 offen
	buffer_load_dword v53, v35, s[4:7], s17 offen
	buffer_load_dword v54, v35, s[4:7], s22 offen
	buffer_load_dword v55, v35, s[4:7], s12 offen
	s_mov_b32 s12, 0x100000
	s_mov_b32 s13, 0x8000
	s_mov_b32 s14, 0x120000
	s_mov_b32 s16, 0x140000
	s_mov_b32 s18, 0x160000
	s_mov_b32 s20, 0x180000
	s_mov_b32 s22, 0x1a0000
	s_mov_b32 s24, 0x1c0000
	s_mov_b32 s26, 0x1e0000
	buffer_load_dword v56, v34, s[8:11], s12 offen
	buffer_load_dword v57, v34, s[8:11], s14 offen
	buffer_load_dword v58, v34, s[8:11], s16 offen
	buffer_load_dword v59, v34, s[8:11], s18 offen
	buffer_load_dword v60, v34, s[8:11], s20 offen
	buffer_load_dword v61, v34, s[8:11], s22 offen
	buffer_load_dword v62, v34, s[8:11], s24 offen
	buffer_load_dword v63, v34, s[8:11], s26 offen
	s_mov_b32 s12, 0xf000
	s_mov_b32 s15, 0x9000
	s_mov_b32 s17, 0xa000
	s_mov_b32 s19, 0xb000
	s_mov_b32 s21, 0xc000
	s_mov_b32 s23, 0xd000
	s_mov_b32 s25, 0xe000
	buffer_load_dword v64, v35, s[4:7], s13 offen
	buffer_load_dword v65, v35, s[4:7], s15 offen
	buffer_load_dword v66, v35, s[4:7], s17 offen
	buffer_load_dword v67, v35, s[4:7], s19 offen
	buffer_load_dword v68, v35, s[4:7], s21 offen
	buffer_load_dword v69, v35, s[4:7], s23 offen
	buffer_load_dword v70, v35, s[4:7], s25 offen
	buffer_load_dword v71, v35, s[4:7], s12 offen
	s_mov_b32 s12, 0x200000
	s_mov_b32 s13, 0x10000
	s_mov_b32 s14, 0x220000
	s_mov_b32 s16, 0x240000
	s_mov_b32 s18, 0x260000
	s_mov_b32 s20, 0x280000
	s_mov_b32 s22, 0x2a0000
	s_mov_b32 s24, 0x2c0000
	s_mov_b32 s26, 0x2e0000
	buffer_load_dword v72, v34, s[8:11], s12 offen
	buffer_load_dword v73, v34, s[8:11], s14 offen
	buffer_load_dword v74, v34, s[8:11], s16 offen
	buffer_load_dword v75, v34, s[8:11], s18 offen
	buffer_load_dword v76, v34, s[8:11], s20 offen
	buffer_load_dword v77, v34, s[8:11], s22 offen
	buffer_load_dword v78, v34, s[8:11], s24 offen
	buffer_load_dword v79, v34, s[8:11], s26 offen
	s_mov_b32 s12, 0x17000
	s_mov_b32 s15, 0x11000
	s_mov_b32 s17, 0x12000
	s_mov_b32 s19, 0x13000
	s_mov_b32 s21, 0x14000
	s_mov_b32 s23, 0x15000
	s_mov_b32 s25, 0x16000
	buffer_load_dword v80, v35, s[4:7], s13 offen
	buffer_load_dword v81, v35, s[4:7], s15 offen
	buffer_load_dword v82, v35, s[4:7], s17 offen
	buffer_load_dword v83, v35, s[4:7], s19 offen
	buffer_load_dword v84, v35, s[4:7], s21 offen
	buffer_load_dword v85, v35, s[4:7], s23 offen
	buffer_load_dword v86, v35, s[4:7], s25 offen
	buffer_load_dword v87, v35, s[4:7], s12 offen
	s_mov_b32 s12, 0x300000
	s_mov_b32 s13, 0x18000
	s_mov_b32 s14, 0x320000
	s_mov_b32 s15, 0x19000
	s_mov_b32 s16, 0x340000
	s_mov_b32 s17, 0x1a000
	s_mov_b32 s18, 0x360000
	s_mov_b32 s19, 0x1b000
	s_mov_b32 s20, 0x380000
	s_mov_b32 s21, 0x1c000
	s_mov_b32 s22, 0x3a0000
	s_mov_b32 s23, 0x1d000
	s_mov_b32 s24, 0x3c0000
	s_mov_b32 s25, 0x1e000
	s_mov_b32 s26, 0x3e0000
	buffer_load_dword v88, v34, s[8:11], s12 offen
	buffer_load_dword v89, v34, s[8:11], s14 offen
	buffer_load_dword v90, v34, s[8:11], s16 offen
	buffer_load_dword v91, v34, s[8:11], s18 offen
	buffer_load_dword v92, v34, s[8:11], s20 offen
	buffer_load_dword v93, v34, s[8:11], s22 offen
	buffer_load_dword v94, v34, s[8:11], s24 offen
	buffer_load_dword v95, v34, s[8:11], s26 offen
	s_mov_b32 s8, 0x1f000
	buffer_load_dword v96, v35, s[4:7], s13 offen
	buffer_load_dword v97, v35, s[4:7], s15 offen
	buffer_load_dword v98, v35, s[4:7], s17 offen
	buffer_load_dword v99, v35, s[4:7], s19 offen
	buffer_load_dword v100, v35, s[4:7], s21 offen
	buffer_load_dword v101, v35, s[4:7], s23 offen
	buffer_load_dword v102, v35, s[4:7], s25 offen
	buffer_load_dword v103, v35, s[4:7], s8 offen
	s_waitcnt vmcnt(62)
	v_cvt_f64_f32_e32 v[38:39], v27
	v_mul_f64 v[38:39], v[38:39], v[38:39]
	v_cvt_f64_f32_e32 v[26:27], v26
	v_fmac_f64_e32 v[38:39], v[26:27], v[26:27]
	v_cvt_f64_f32_e32 v[26:27], v28
	v_fmac_f64_e32 v[38:39], v[26:27], v[26:27]
	v_cvt_f64_f32_e32 v[26:27], v29
	v_fmac_f64_e32 v[38:39], v[26:27], v[26:27]
	v_cvt_f64_f32_e32 v[26:27], v23
	v_mul_f64 v[26:27], v[26:27], v[26:27]
	v_cvt_f64_f32_e32 v[22:23], v22
	v_fmac_f64_e32 v[26:27], v[22:23], v[22:23]
	v_cvt_f64_f32_e32 v[22:23], v24
	v_fmac_f64_e32 v[26:27], v[22:23], v[22:23]
	v_cvt_f64_f32_e32 v[22:23], v25
	v_fmac_f64_e32 v[26:27], v[22:23], v[22:23]
	v_cvt_f64_f32_e32 v[22:23], v19
	v_mul_f64 v[22:23], v[22:23], v[22:23]
	v_cvt_f64_f32_e32 v[18:19], v18
	v_fmac_f64_e32 v[22:23], v[18:19], v[18:19]
	v_cvt_f64_f32_e32 v[18:19], v20
	v_fmac_f64_e32 v[22:23], v[18:19], v[18:19]
	v_cvt_f64_f32_e32 v[18:19], v21
	v_fmac_f64_e32 v[22:23], v[18:19], v[18:19]
	v_cvt_f64_f32_e32 v[18:19], v15
	v_mul_f64 v[18:19], v[18:19], v[18:19]
	v_cvt_f64_f32_e32 v[14:15], v14
	v_fmac_f64_e32 v[18:19], v[14:15], v[14:15]
	v_cvt_f64_f32_e32 v[14:15], v16
	v_fmac_f64_e32 v[18:19], v[14:15], v[14:15]
	v_cvt_f64_f32_e32 v[14:15], v17
	v_fmac_f64_e32 v[18:19], v[14:15], v[14:15]
	v_cvt_f64_f32_e32 v[14:15], v11
	v_mul_f64 v[14:15], v[14:15], v[14:15]
	v_cvt_f64_f32_e32 v[10:11], v10
	v_fmac_f64_e32 v[14:15], v[10:11], v[10:11]
	v_cvt_f64_f32_e32 v[10:11], v12
	v_fmac_f64_e32 v[14:15], v[10:11], v[10:11]
	v_cvt_f64_f32_e32 v[10:11], v13
	v_fmac_f64_e32 v[14:15], v[10:11], v[10:11]
	v_cvt_f64_f32_e32 v[10:11], v7
	v_mul_f64 v[10:11], v[10:11], v[10:11]
	v_cvt_f64_f32_e32 v[6:7], v6
	v_fmac_f64_e32 v[10:11], v[6:7], v[6:7]
	v_cvt_f64_f32_e32 v[6:7], v8
	v_fmac_f64_e32 v[10:11], v[6:7], v[6:7]
	v_cvt_f64_f32_e32 v[6:7], v9
	v_fmac_f64_e32 v[10:11], v[6:7], v[6:7]
	v_cvt_f64_f32_e32 v[6:7], v3
	v_mul_f64 v[6:7], v[6:7], v[6:7]
	v_cvt_f64_f32_e32 v[2:3], v2
	v_fmac_f64_e32 v[6:7], v[2:3], v[2:3]
	v_cvt_f64_f32_e32 v[2:3], v4
	v_fmac_f64_e32 v[6:7], v[2:3], v[2:3]
	v_cvt_f64_f32_e32 v[2:3], v5
	v_fmac_f64_e32 v[6:7], v[2:3], v[2:3]
	v_cvt_f64_f32_e32 v[2:3], v40
	v_add_f64 v[2:3], v[2:3], 0
	s_waitcnt vmcnt(59)
	v_cvt_f64_f32_e32 v[4:5], v44
	v_add_f64 v[2:3], v[2:3], v[4:5]
	s_waitcnt vmcnt(55)
	v_cvt_f64_f32_e32 v[4:5], v48
	v_add_f64 v[4:5], v[4:5], 0
	s_waitcnt vmcnt(51)
	v_cvt_f64_f32_e32 v[8:9], v52
	v_add_f64 v[4:5], v[4:5], v[8:9]
	v_cvt_f64_f32_e32 v[8:9], v41
	v_add_f64 v[8:9], v[8:9], 0
	v_cvt_f64_f32_e32 v[12:13], v45
	v_add_f64 v[8:9], v[8:9], v[12:13]
	v_cvt_f64_f32_e32 v[12:13], v49
	v_add_f64 v[12:13], v[12:13], 0
	s_waitcnt vmcnt(50)
	v_cvt_f64_f32_e32 v[16:17], v53
	v_add_f64 v[12:13], v[12:13], v[16:17]
	v_cvt_f64_f32_e32 v[16:17], v42
	v_add_f64 v[16:17], v[16:17], 0
	v_cvt_f64_f32_e32 v[20:21], v46
	v_add_f64 v[16:17], v[16:17], v[20:21]
	v_cvt_f64_f32_e32 v[20:21], v50
	v_add_f64 v[20:21], v[20:21], 0
	s_waitcnt vmcnt(49)
	v_cvt_f64_f32_e32 v[24:25], v54
	v_add_f64 v[20:21], v[20:21], v[24:25]
	v_cvt_f64_f32_e32 v[24:25], v43
	v_add_f64 v[24:25], v[24:25], 0
	v_cvt_f64_f32_e32 v[28:29], v47
	v_add_f64 v[24:25], v[24:25], v[28:29]
	v_cvt_f64_f32_e32 v[28:29], v51
	v_add_f64 v[28:29], v[28:29], 0
	s_waitcnt vmcnt(48)
	v_cvt_f64_f32_e32 v[40:41], v55
	v_add_f64 v[28:29], v[28:29], v[40:41]
	s_waitcnt vmcnt(47)
	v_cvt_f64_f32_e32 v[40:41], v56
	v_add_f64 v[2:3], v[2:3], v[40:41]
	s_waitcnt vmcnt(39)
	v_cvt_f64_f32_e32 v[40:41], v64
	v_add_f64 v[4:5], v[4:5], v[40:41]
	v_cvt_f64_f32_e32 v[40:41], v57
	v_add_f64 v[8:9], v[8:9], v[40:41]
	s_waitcnt vmcnt(38)
	v_cvt_f64_f32_e32 v[40:41], v65
	v_add_f64 v[12:13], v[12:13], v[40:41]
	v_cvt_f64_f32_e32 v[40:41], v58
	v_add_f64 v[16:17], v[16:17], v[40:41]
	s_waitcnt vmcnt(37)
	v_cvt_f64_f32_e32 v[40:41], v66
	v_add_f64 v[20:21], v[20:21], v[40:41]
	v_cvt_f64_f32_e32 v[40:41], v59
	v_add_f64 v[24:25], v[24:25], v[40:41]
	s_waitcnt vmcnt(36)
	v_cvt_f64_f32_e32 v[40:41], v67
	v_add_f64 v[28:29], v[28:29], v[40:41]
	v_cvt_f64_f32_e32 v[40:41], v60
	v_add_f64 v[2:3], v[2:3], v[40:41]
	s_waitcnt vmcnt(35)
	v_cvt_f64_f32_e32 v[40:41], v68
	v_add_f64 v[4:5], v[4:5], v[40:41]
	v_cvt_f64_f32_e32 v[40:41], v61
	v_add_f64 v[8:9], v[8:9], v[40:41]
	s_waitcnt vmcnt(34)
	v_cvt_f64_f32_e32 v[40:41], v69
	v_add_f64 v[12:13], v[12:13], v[40:41]
	v_cvt_f64_f32_e32 v[40:41], v62
	v_add_f64 v[16:17], v[16:17], v[40:41]
	s_waitcnt vmcnt(33)
	v_cvt_f64_f32_e32 v[40:41], v70
	v_add_f64 v[20:21], v[20:21], v[40:41]
	v_cvt_f64_f32_e32 v[40:41], v63
	v_add_f64 v[24:25], v[24:25], v[40:41]
	s_waitcnt vmcnt(32)
	v_cvt_f64_f32_e32 v[40:41], v71
	v_add_f64 v[28:29], v[28:29], v[40:41]
	s_waitcnt vmcnt(31)
	v_cvt_f64_f32_e32 v[40:41], v72
	v_add_f64 v[2:3], v[2:3], v[40:41]
	s_waitcnt vmcnt(23)
	v_cvt_f64_f32_e32 v[40:41], v80
	v_add_f64 v[4:5], v[4:5], v[40:41]
	v_cvt_f64_f32_e32 v[40:41], v73
	v_add_f64 v[8:9], v[8:9], v[40:41]
	s_waitcnt vmcnt(22)
	v_cvt_f64_f32_e32 v[40:41], v81
	v_add_f64 v[12:13], v[12:13], v[40:41]
	v_cvt_f64_f32_e32 v[40:41], v74
	v_add_f64 v[16:17], v[16:17], v[40:41]
	s_waitcnt vmcnt(21)
	v_cvt_f64_f32_e32 v[40:41], v82
	v_add_f64 v[20:21], v[20:21], v[40:41]
	v_cvt_f64_f32_e32 v[40:41], v75
	v_add_f64 v[24:25], v[24:25], v[40:41]
	s_waitcnt vmcnt(20)
	v_cvt_f64_f32_e32 v[40:41], v83
	v_add_f64 v[28:29], v[28:29], v[40:41]
	v_cvt_f64_f32_e32 v[40:41], v76
	v_add_f64 v[2:3], v[2:3], v[40:41]
	s_waitcnt vmcnt(19)
	v_cvt_f64_f32_e32 v[40:41], v84
	v_add_f64 v[4:5], v[4:5], v[40:41]
	v_cvt_f64_f32_e32 v[40:41], v77
	v_add_f64 v[8:9], v[8:9], v[40:41]
	s_waitcnt vmcnt(18)
	v_cvt_f64_f32_e32 v[40:41], v85
	v_add_f64 v[12:13], v[12:13], v[40:41]
	v_cvt_f64_f32_e32 v[40:41], v78
	v_add_f64 v[16:17], v[16:17], v[40:41]
	s_waitcnt vmcnt(17)
	v_cvt_f64_f32_e32 v[40:41], v86
	v_add_f64 v[20:21], v[20:21], v[40:41]
	v_cvt_f64_f32_e32 v[40:41], v79
	v_add_f64 v[24:25], v[24:25], v[40:41]
	s_waitcnt vmcnt(16)
	v_cvt_f64_f32_e32 v[40:41], v87
	v_add_f64 v[28:29], v[28:29], v[40:41]
	s_waitcnt vmcnt(15)
	v_cvt_f64_f32_e32 v[40:41], v88
	v_add_f64 v[2:3], v[2:3], v[40:41]
	s_waitcnt vmcnt(7)
	v_cvt_f64_f32_e32 v[40:41], v96
	v_add_f64 v[4:5], v[4:5], v[40:41]
	v_cvt_f64_f32_e32 v[40:41], v89
	v_add_f64 v[8:9], v[8:9], v[40:41]
	s_waitcnt vmcnt(6)
	v_cvt_f64_f32_e32 v[40:41], v97
	v_add_f64 v[12:13], v[12:13], v[40:41]
	v_cvt_f64_f32_e32 v[40:41], v90
	v_add_f64 v[16:17], v[16:17], v[40:41]
	s_waitcnt vmcnt(5)
	v_cvt_f64_f32_e32 v[40:41], v98
	v_add_f64 v[20:21], v[20:21], v[40:41]
	v_cvt_f64_f32_e32 v[40:41], v91
	v_add_f64 v[24:25], v[24:25], v[40:41]
	s_waitcnt vmcnt(4)
	v_cvt_f64_f32_e32 v[40:41], v99
	v_add_f64 v[28:29], v[28:29], v[40:41]
	v_cvt_f64_f32_e32 v[40:41], v92
	v_add_f64 v[2:3], v[2:3], v[40:41]
	s_waitcnt vmcnt(3)
	v_cvt_f64_f32_e32 v[40:41], v100
	v_add_f64 v[4:5], v[4:5], v[40:41]
	v_cvt_f64_f32_e32 v[40:41], v93
	v_add_f64 v[8:9], v[8:9], v[40:41]
	s_waitcnt vmcnt(2)
	v_cvt_f64_f32_e32 v[40:41], v101
	v_add_f64 v[12:13], v[12:13], v[40:41]
	v_cvt_f64_f32_e32 v[40:41], v94
	v_add_f64 v[16:17], v[16:17], v[40:41]
	s_waitcnt vmcnt(1)
	v_cvt_f64_f32_e32 v[40:41], v102
	v_add_f64 v[20:21], v[20:21], v[40:41]
	v_cvt_f64_f32_e32 v[40:41], v95
	v_add_f64 v[24:25], v[24:25], v[40:41]
	s_waitcnt vmcnt(0)
	v_cvt_f64_f32_e32 v[40:41], v103
	v_add_f64 v[28:29], v[28:29], v[40:41]
	v_add_f64 v[2:3], v[2:3], v[8:9]
	v_add_f64 v[8:9], v[16:17], v[24:25]
	v_add_f64 v[2:3], v[2:3], v[8:9]
	v_add_f64 v[4:5], v[4:5], v[12:13]
	v_add_f64 v[8:9], v[20:21], v[28:29]
	v_add_f64 v[4:5], v[4:5], v[8:9]
	s_mov_b32 s4, 0
	v_fmac_f64_e32 v[4:5], -2.0, v[2:3]
	s_mov_b32 s5, 0xc0df4000
	v_add_f64 v[2:3], v[4:5], s[4:5]
	v_cvt_f32_f64_e32 v3, v[2:3]
	v_cvt_f64_f32_e32 v[34:35], v30
	v_cvt_f64_f32_e32 v[30:31], v31
	v_mov_b32_dpp v2, v3 quad_perm:[1,0,3,2] row_mask:0xf bank_mask:0xf bound_ctrl:1
	v_max_f32_e32 v2, v2, v2
	v_min_f32_e32 v2, v3, v2
	v_mul_f64 v[30:31], v[30:31], v[30:31]
	v_cvt_f64_f32_e32 v[36:37], v32
	v_mov_b32_dpp v4, v2 quad_perm:[2,3,0,1] row_mask:0xf bank_mask:0xf bound_ctrl:1
	v_max_f32_e32 v4, v4, v4
	v_min_f32_e32 v2, v2, v4
	v_fmac_f64_e32 v[30:31], v[34:35], v[34:35]
	v_cvt_f64_f32_e32 v[32:33], v33
	v_mov_b32_dpp v4, v2 row_half_mirror row_mask:0xf bank_mask:0xf bound_ctrl:1
	v_fmac_f64_e32 v[30:31], v[36:37], v[36:37]
	v_max_f32_e32 v4, v4, v4
	v_fmac_f64_e32 v[30:31], v[32:33], v[32:33]
	v_min_f32_e32 v2, v2, v4
	v_add_f64 v[30:31], v[30:31], v[38:39]
	v_add_f64 v[26:27], v[30:31], v[26:27]
	v_mov_b32_dpp v4, v2 row_mirror row_mask:0xf bank_mask:0xf bound_ctrl:1
	v_max_f32_e32 v4, v4, v4
	v_add_f64 v[22:23], v[26:27], v[22:23]
	v_min_f32_e32 v2, v2, v4
	v_add_f64 v[18:19], v[22:23], v[18:19]
	v_readlane_b32 s6, v2, 32
	v_readlane_b32 s7, v2, 48
	v_add_f64 v[14:15], v[18:19], v[14:15]
	v_readlane_b32 s4, v2, 0
	v_readlane_b32 s5, v2, 16
	v_max_f32_e64 v2, s7, s7
	v_max_f32_e64 v4, s6, s6
	v_add_f64 v[10:11], v[14:15], v[10:11]
	v_min_f32_e32 v2, v4, v2
	v_mov_b32_e32 v4, s5
	v_add_f64 v[6:7], v[10:11], v[6:7]
	v_min3_f32 v2, s4, v4, v2
	v_cmp_eq_f32_e32 vcc, v2, v3
	v_cvt_f32_f64_e32 v3, v[6:7]
	s_nop 1
	v_add_f32_dpp v3, v3, v3 quad_perm:[1,0,3,2] row_mask:0xf bank_mask:0xf bound_ctrl:1
	s_nop 1
	v_add_f32_dpp v3, v3, v3 quad_perm:[2,3,0,1] row_mask:0xf bank_mask:0xf bound_ctrl:1
	s_nop 1
	v_add_f32_dpp v3, v3, v3 row_half_mirror row_mask:0xf bank_mask:0xf bound_ctrl:1
	s_nop 1
	v_add_f32_dpp v3, v3, v3 row_mirror row_mask:0xf bank_mask:0xf bound_ctrl:1
	s_nop 0
	v_readlane_b32 s8, v3, 0
	v_readlane_b32 s10, v3, 16
	v_readlane_b32 s9, v3, 32
	v_readlane_b32 s11, v3, 48
	v_and_b32_e32 v3, 63, v0
	v_cmp_eq_u32_e64 s[4:5], 0, v3
	s_and_saveexec_b64 s[6:7], s[4:5]
	s_cbranch_execz .LBB1_2
	v_mov_b32_e32 v4, s10
	v_mov_b32_e32 v5, s11
	s_ff1_i32_b64 s4, vcc
	v_pk_add_f32 v[4:5], s[8:9], v[4:5]
	v_and_or_b32 v3, v0, 64, s4
	v_add_f32_e32 v4, v4, v5
	v_or_b32_e32 v5, s3, v3
	v_lshrrev_b32_e32 v6, 4, v0
	v_cvt_f64_f32_e32 v[2:3], v2
	ds_write_b32 v6, v5 offset:32
	v_cvt_f64_f32_e32 v[4:5], v4
	ds_write2_b64 v1, v[2:3], v[4:5] offset1:2
.LBB1_2:
	s_or_b64 exec, exec, s[6:7]
	v_cmp_eq_u32_e32 vcc, 0, v0
	s_waitcnt lgkmcnt(0)
	s_barrier
	s_and_saveexec_b64 s[4:5], vcc
	s_cbranch_execz .LBB1_4
	v_mov_b32_e32 v10, 0
	ds_read_b128 v[0:3], v10
	s_mov_b64 s[4:5], s[28:29]
	s_mov_b64 s[6:7], s[30:31]
	s_mov_b64 s[8:9], s[32:33]
	s_mov_b32 s0, 0
	s_mov_b32 s1, 0x40df4000
	s_mov_b32 s3, 0
	s_waitcnt lgkmcnt(0)
	v_cmp_lt_f64_e32 vcc, v[2:3], v[0:1]
	ds_read_b64 v[8:9], v10 offset:32
	ds_read_b128 v[4:7], v10 offset:16
	v_cndmask_b32_e32 v1, v1, v3, vcc
	v_cndmask_b32_e32 v0, v0, v2, vcc
	v_add_f64 v[0:1], v[0:1], s[0:1]
	s_lshl_b64 s[0:1], s[2:3], 3
	s_add_u32 s4, s4, s0
	s_addc_u32 s5, s5, s1
	s_lshl_b64 s[2:3], s[2:3], 2
	s_add_u32 s2, s6, s2
	s_addc_u32 s3, s7, s3
	s_add_u32 s0, s8, s0
	s_waitcnt lgkmcnt(1)
	v_cndmask_b32_e32 v2, v8, v9, vcc
	global_store_dwordx2 v10, v[0:1], s[4:5]
	s_waitcnt lgkmcnt(0)
	v_add_f64 v[0:1], v[4:5], v[6:7]
	s_addc_u32 s1, s9, s1
	global_store_dword v10, v2, s[2:3]
	global_store_dwordx2 v10, v[0:1], s[0:1]

	.amdhsa_kernel _Z9k2_reducePKfS0_S0_PdPiS1_
		.amdhsa_group_segment_fixed_size 40
		.amdhsa_private_segment_fixed_size 0
		.amdhsa_kernarg_size 48
		.amdhsa_user_sgpr_count 2
		.amdhsa_user_sgpr_dispatch_ptr 0
		.amdhsa_user_sgpr_queue_ptr 0
		.amdhsa_user_sgpr_kernarg_segment_ptr 1
		.amdhsa_user_sgpr_dispatch_id 0
		.amdhsa_user_sgpr_kernarg_preload_length 0
		.amdhsa_user_sgpr_kernarg_preload_offset 0
		.amdhsa_user_sgpr_private_segment_size 0
		.amdhsa_uses_dynamic_stack 0
		.amdhsa_enable_private_segment 0
		.amdhsa_system_sgpr_workgroup_id_x 1
		.amdhsa_system_sgpr_workgroup_id_y 0
		.amdhsa_system_sgpr_workgroup_id_z 0
		.amdhsa_system_sgpr_workgroup_info 0
		.amdhsa_system_vgpr_workitem_id 0
		.amdhsa_next_free_vgpr 104
		.amdhsa_next_free_sgpr 34
		.amdhsa_accum_offset 104
		.amdhsa_reserve_vcc 1
		.amdhsa_float_round_mode_32 0
		.amdhsa_float_round_mode_16_64 0
		.amdhsa_float_denorm_mode_32 3
		.amdhsa_float_denorm_mode_16_64 3
		.amdhsa_dx10_clamp 1
		.amdhsa_ieee_mode 1
		.amdhsa_fp16_overflow 0
		.amdhsa_tg_split 0
		.amdhsa_exception_fp_ieee_invalid_op 0
		.amdhsa_exception_fp_denorm_src 0
		.amdhsa_exception_fp_ieee_div_zero 0
		.amdhsa_exception_fp_ieee_overflow 0
		.amdhsa_exception_fp_ieee_underflow 0
		.amdhsa_exception_fp_ieee_inexact 0
		.amdhsa_exception_int_div_zero 0
	.end_amdhsa_kernel

_Z9k3_gatherPKfS0_PKdPKiS2_Pf:
	s_load_dwordx4 s[4:7], s[0:1], 0x10
	s_load_dwordx2 s[8:9], s[0:1], 0x28
	s_load_dwordx2 s[18:19], s[0:1], 0x0
	s_load_dwordx2 s[20:21], s[0:1], 0x8
	s_cmpk_gt_u32 s2, 0x1ff
	s_mov_b64 s[10:11], -1
	s_cbranch_scc0 .LBB2_19
	s_load_dwordx2 s[10:11], s[0:1], 0x20
	v_lshlrev_b32_e32 v6, 3, v0
	s_waitcnt lgkmcnt(0)
	s_lshl_b32 s22, s2, 9
	s_add_u32 s22, s22, 0xfffc0000
	s_add_u32 s20, s20, s22
	s_addc_u32 s21, s21, 0
	v_lshlrev_b32_e32 v22, 2, v0
	v_cmp_gt_u32_e32 vcc, 0x80, v0
	s_and_saveexec_b64 s[22:23], vcc
	global_load_dword v23, v22, s[20:21]
	s_mov_b64 exec, s[22:23]
	global_load_dwordx2 v[4:5], v6, s[4:5]
	v_lshlrev_b32_e32 v7, 2, v0
	global_load_dword v1, v7, s[6:7]
	global_load_dwordx2 v[2:3], v6, s[10:11]
	s_mov_b64 s[10:11], -1
	s_mov_b64 s[14:15], -1
	s_waitcnt vmcnt(2)
	v_mov_b32_dpp v6, v4 quad_perm:[1,0,3,2] row_mask:0xf bank_mask:0xf bound_ctrl:1
	v_mov_b32_dpp v7, v5 quad_perm:[1,0,3,2] row_mask:0xf bank_mask:0xf bound_ctrl:1
	s_waitcnt vmcnt(1)
	v_mov_b32_dpp v8, v1 quad_perm:[1,0,3,2] row_mask:0xf bank_mask:0xf bound_ctrl:1
	v_cmp_ngt_f64_e32 vcc, v[4:5], v[6:7]
	s_and_saveexec_b64 s[12:13], vcc
	s_cbranch_execz .LBB2_5
	v_cmp_eq_f64_e32 vcc, v[4:5], v[6:7]
	s_mov_b64 s[14:15], 0
	s_and_saveexec_b64 s[16:17], vcc
	v_cmp_lt_i32_e32 vcc, v8, v1
	s_and_b64 s[14:15], vcc, exec
	s_or_b64 exec, exec, s[16:17]
	s_orn2_b64 s[14:15], s[14:15], exec

.LBB2_16:
	s_or_b64 exec, exec, s[10:11]
	s_movk_i32 s10, 0x80
	v_cmp_gt_u32_e32 vcc, s10, v0
	s_waitcnt lgkmcnt(0)
	s_barrier
	s_and_saveexec_b64 s[10:11], vcc
	s_cbranch_execz .LBB2_18
	v_mov_b32_e32 v1, 0
	ds_read_b128 v[2:5], v1
	v_lshl_or_b32 v18, s3, 7, v0
	ds_read_b128 v[6:9], v1 offset:16
	ds_read_b128 v[10:13], v1 offset:32
	ds_read_b128 v[14:17], v1 offset:48
	v_ashrrev_i32_e32 v19, 31, v18
	s_waitcnt lgkmcnt(0)
	v_cmp_eq_u32_e32 vcc, v2, v18
	v_lshlrev_b64 v[20:21], 2, v[18:19]
	s_nop 0
	v_cndmask_b32_e64 v2, 0, 1.0, vcc
	v_cmp_eq_u32_e32 vcc, v3, v18
	s_nop 1
	v_cndmask_b32_e64 v3, 0, 1.0, vcc
	v_cmp_eq_u32_e32 vcc, v4, v18
	v_add_f32_e32 v2, v2, v3
	s_nop 0
	v_cndmask_b32_e64 v3, 0, 1.0, vcc
	v_cmp_eq_u32_e32 vcc, v5, v18
	v_add_f32_e32 v2, v2, v3
	s_nop 0
	v_cndmask_b32_e64 v3, 0, 1.0, vcc
	v_cmp_eq_u32_e32 vcc, v6, v18
	v_add_f32_e32 v2, v2, v3
	s_nop 0
	v_cndmask_b32_e64 v3, 0, 1.0, vcc
	v_cmp_eq_u32_e32 vcc, v7, v18
	v_add_f32_e32 v2, v2, v3
	s_nop 0
	v_cndmask_b32_e64 v3, 0, 1.0, vcc
	v_cmp_eq_u32_e32 vcc, v8, v18
	v_add_f32_e32 v2, v2, v3
	s_nop 0
	v_cndmask_b32_e64 v3, 0, 1.0, vcc
	v_add_f32_e32 v4, v2, v3
	v_cmp_eq_u32_e32 vcc, v9, v18
	s_nop 1
	v_cndmask_b32_e64 v2, 0, 1.0, vcc
	v_cmp_eq_u32_e32 vcc, v10, v18
	v_add_f32_e32 v2, v4, v2
	s_nop 0
	v_cndmask_b32_e64 v3, 0, 1.0, vcc
	v_cmp_eq_u32_e32 vcc, v11, v18
	v_add_f32_e32 v2, v2, v3
	s_nop 0
	v_cndmask_b32_e64 v3, 0, 1.0, vcc
	v_cmp_eq_u32_e32 vcc, v12, v18
	v_add_f32_e32 v2, v2, v3
	s_nop 0
	v_cndmask_b32_e64 v3, 0, 1.0, vcc
	v_cmp_eq_u32_e32 vcc, v13, v18
	v_add_f32_e32 v2, v2, v3
	s_nop 0
	v_cndmask_b32_e64 v3, 0, 1.0, vcc
	v_cmp_eq_u32_e32 vcc, v14, v18
	v_add_f32_e32 v2, v2, v3
	s_nop 0
	v_cndmask_b32_e64 v3, 0, 1.0, vcc
	v_cmp_eq_u32_e32 vcc, v15, v18
	v_add_f32_e32 v2, v2, v3
	s_nop 0
	v_cndmask_b32_e64 v3, 0, 1.0, vcc
	v_cmp_eq_u32_e32 vcc, v16, v18
	v_add_f32_e32 v2, v2, v3
	s_nop 0
	v_cndmask_b32_e64 v3, 0, 1.0, vcc
	v_add_f32_e32 v6, v2, v3
	ds_read_b128 v[2:5], v1 offset:64
	v_cmp_eq_u32_e32 vcc, v17, v18
	s_nop 1
	v_cndmask_b32_e64 v7, 0, 1.0, vcc
	v_add_f32_e32 v10, v6, v7
	ds_read_b128 v[6:9], v1 offset:80
	s_waitcnt lgkmcnt(1)
	v_cmp_eq_u32_e32 vcc, v2, v18
	s_nop 1
	v_cndmask_b32_e64 v2, 0, 1.0, vcc
	v_cmp_eq_u32_e32 vcc, v3, v18
	v_add_f32_e32 v2, v10, v2
	s_nop 0
	v_cndmask_b32_e64 v3, 0, 1.0, vcc
	v_cmp_eq_u32_e32 vcc, v4, v18
	v_add_f32_e32 v2, v2, v3
	s_nop 0
	v_cndmask_b32_e64 v3, 0, 1.0, vcc
	v_cmp_eq_u32_e32 vcc, v5, v18
	v_add_f32_e32 v2, v2, v3
	s_nop 0
	v_cndmask_b32_e64 v3, 0, 1.0, vcc
	s_waitcnt lgkmcnt(0)
	v_cmp_eq_u32_e32 vcc, v6, v18
	v_add_f32_e32 v2, v2, v3
	s_nop 0
	v_cndmask_b32_e64 v3, 0, 1.0, vcc
	v_cmp_eq_u32_e32 vcc, v7, v18
	v_add_f32_e32 v2, v2, v3
	s_nop 0
	v_cndmask_b32_e64 v3, 0, 1.0, vcc
	v_cmp_eq_u32_e32 vcc, v8, v18
	v_add_f32_e32 v2, v2, v3
	s_nop 0
	v_cndmask_b32_e64 v3, 0, 1.0, vcc
	v_add_f32_e32 v6, v2, v3
	ds_read_b128 v[2:5], v1 offset:96
	v_cmp_eq_u32_e32 vcc, v9, v18
	s_nop 1
	v_cndmask_b32_e64 v7, 0, 1.0, vcc
	v_add_f32_e32 v10, v6, v7
	ds_read_b128 v[6:9], v1 offset:112
	s_waitcnt lgkmcnt(1)
	v_cmp_eq_u32_e32 vcc, v2, v18
	s_nop 1
	v_cndmask_b32_e64 v1, 0, 1.0, vcc
	v_cmp_eq_u32_e32 vcc, v3, v18
	v_add_f32_e32 v1, v10, v1
	s_nop 0
	v_cndmask_b32_e64 v2, 0, 1.0, vcc
	v_cmp_eq_u32_e32 vcc, v4, v18
	v_add_f32_e32 v1, v1, v2
	s_nop 0
	v_cndmask_b32_e64 v2, 0, 1.0, vcc
	v_cmp_eq_u32_e32 vcc, v5, v18
	v_add_f32_e32 v1, v1, v2
	s_nop 0
	v_cndmask_b32_e64 v2, 0, 1.0, vcc
	s_waitcnt lgkmcnt(0)
	v_cmp_eq_u32_e32 vcc, v6, v18
	v_add_f32_e32 v1, v1, v2
	s_nop 0
	v_cndmask_b32_e64 v2, 0, 1.0, vcc
	v_cmp_eq_u32_e32 vcc, v7, v18
	v_add_f32_e32 v1, v1, v2
	s_nop 0
	v_cndmask_b32_e64 v2, 0, 1.0, vcc
	v_cmp_eq_u32_e32 vcc, v8, v18
	v_add_f32_e32 v1, v1, v2
	s_nop 0
	v_cndmask_b32_e64 v2, 0, 1.0, vcc
	v_cmp_eq_u32_e32 vcc, v9, v18
	v_add_f32_e32 v1, v1, v2
	s_nop 0
	v_cndmask_b32_e64 v2, 0, 1.0, vcc
	v_add_f32_e32 v1, v1, v2
	v_lshl_add_u64 v[2:3], s[8:9], 0, v[20:21]
	v_add_co_u32_e32 v2, vcc, 0x3e8000, v2
	s_waitcnt vmcnt(0)
	v_add_f32_e32 v1, v1, v23
	v_addc_co_u32_e32 v3, vcc, 0, v3, vcc
	global_store_dword v[2:3], v1, off offset:256

.LBB2_32:
	s_or_b64 exec, exec, s[4:5]
	s_mul_i32 s3, s3, 0x1f400
	v_readfirstlane_b32 s4, v6
	s_and_b32 s2, s2, 15
	s_mul_i32 s6, s2, 0x1f40
	s_add_u32 s2, s8, s3
	s_addc_u32 s3, s9, 0
	s_add_u32 s2, s2, s6
	s_addc_u32 s3, s3, 0
	s_mul_hi_i32 s5, s4, 0x1f400
	s_mul_i32 s4, s4, 0x1f400
	s_add_u32 s4, s4, s6
	s_addc_u32 s5, s5, 0
	s_add_u32 s0, s18, s4
	s_addc_u32 s1, s19, s5
	v_lshlrev_b32_e32 v2, 4, v0
	v_cmp_gt_u32_e32 vcc, 0xf4, v0
	global_load_dwordx4 v[6:9], v2, s[0:1] nt
	s_add_u32 s0, s0, 0x1000
	s_addc_u32 s1, s1, 0
	s_and_saveexec_b64 s[6:7], vcc
	global_load_dwordx4 v[10:13], v2, s[0:1] nt
	s_mov_b64 exec, s[6:7]
	s_waitcnt vmcnt(1)
	global_store_dwordx4 v2, v[6:9], s[2:3] offset:128 nt
	s_add_u32 s2, s2, 0x1000
	s_addc_u32 s3, s3, 0
	s_and_b64 exec, exec, vcc
	s_waitcnt vmcnt(1)
	global_store_dwordx4 v2, v[10:13], s[2:3] offset:128 nt

	.amdhsa_kernel _Z9k3_gatherPKfS0_PKdPKiS2_Pf
		.amdhsa_group_segment_fixed_size 128
		.amdhsa_private_segment_fixed_size 0
		.amdhsa_kernarg_size 48
		.amdhsa_user_sgpr_count 2
		.amdhsa_user_sgpr_dispatch_ptr 0
		.amdhsa_user_sgpr_queue_ptr 0
		.amdhsa_user_sgpr_kernarg_segment_ptr 1
		.amdhsa_user_sgpr_dispatch_id 0
		.amdhsa_user_sgpr_kernarg_preload_length 0
		.amdhsa_user_sgpr_kernarg_preload_offset 0
		.amdhsa_user_sgpr_private_segment_size 0
		.amdhsa_uses_dynamic_stack 0
		.amdhsa_enable_private_segment 0
		.amdhsa_system_sgpr_workgroup_id_x 1
		.amdhsa_system_sgpr_workgroup_id_y 0
		.amdhsa_system_sgpr_workgroup_id_z 0
		.amdhsa_system_sgpr_workgroup_info 0
		.amdhsa_system_vgpr_workitem_id 0
		.amdhsa_next_free_vgpr 24
		.amdhsa_next_free_sgpr 24
		.amdhsa_accum_offset 24
		.amdhsa_reserve_vcc 1
		.amdhsa_float_round_mode_32 0
		.amdhsa_float_round_mode_16_64 0
		.amdhsa_float_denorm_mode_32 3
		.amdhsa_float_denorm_mode_16_64 3
		.amdhsa_dx10_clamp 1
		.amdhsa_ieee_mode 1
		.amdhsa_fp16_overflow 0
		.amdhsa_tg_split 0
		.amdhsa_exception_fp_ieee_invalid_op 0
		.amdhsa_exception_fp_denorm_src 0
		.amdhsa_exception_fp_ieee_div_zero 0
		.amdhsa_exception_fp_ieee_overflow 0
		.amdhsa_exception_fp_ieee_underflow 0
		.amdhsa_exception_fp_ieee_inexact 0
		.amdhsa_exception_int_div_zero 0
	.end_amdhsa_kernel

amdhsa.kernels:
  - .agpr_count:     0
    .args:
      - .actual_access:  read_only
        .address_space:  global
        .offset:         0
        .size:           8
        .value_kind:     global_buffer
      - .actual_access:  read_only
        .address_space:  global
        .offset:         8
        .size:           8
        .value_kind:     global_buffer
      - .actual_access:  write_only
        .address_space:  global
        .offset:         16
        .size:           8
        .value_kind:     global_buffer
      - .actual_access:  write_only
        .address_space:  global
        .offset:         24
        .size:           8
        .value_kind:     global_buffer
    .group_segment_fixed_size: 141312
    .kernarg_segment_align: 8
    .kernarg_segment_size: 32
    .language:       OpenCL C
    .language_version:
      - 2
      - 0
    .max_flat_workgroup_size: 512
    .name:           _Z9k1_streamPKfS0_PfS1_
    .private_segment_fixed_size: 0
    .sgpr_count:     26
    .sgpr_spill_count: 0
    .symbol:         _Z9k1_streamPKfS0_PfS1_.kd
    .uniform_work_group_size: 1
    .uses_dynamic_stack: false
    .vgpr_count:     210
    .vgpr_spill_count: 0
    .wavefront_size: 64
  - .agpr_count:     0
    .args:
      - .actual_access:  read_only
        .address_space:  global
        .offset:         0
        .size:           8
        .value_kind:     global_buffer
      - .actual_access:  read_only
        .address_space:  global
        .offset:         8
        .size:           8
        .value_kind:     global_buffer
      - .actual_access:  read_only
        .address_space:  global
        .offset:         16
        .size:           8
        .value_kind:     global_buffer
      - .actual_access:  write_only
        .address_space:  global
        .offset:         24
        .size:           8
        .value_kind:     global_buffer
      - .actual_access:  write_only
        .address_space:  global
        .offset:         32
        .size:           8
        .value_kind:     global_buffer
      - .actual_access:  write_only
        .address_space:  global
        .offset:         40
        .size:           8
        .value_kind:     global_buffer
    .group_segment_fixed_size: 40
    .kernarg_segment_align: 8
    .kernarg_segment_size: 48
    .language:       OpenCL C
    .language_version:
      - 2
      - 0
    .max_flat_workgroup_size: 128
    .name:           _Z9k2_reducePKfS0_S0_PdPiS1_
    .private_segment_fixed_size: 0
    .sgpr_count:     40
    .sgpr_spill_count: 0
    .symbol:         _Z9k2_reducePKfS0_S0_PdPiS1_.kd
    .uniform_work_group_size: 1
    .uses_dynamic_stack: false
    .vgpr_count:     104
    .vgpr_spill_count: 0
    .wavefront_size: 64
  - .agpr_count:     0
    .args:
      - .actual_access:  read_only
        .address_space:  global
        .offset:         0
        .size:           8
        .value_kind:     global_buffer
      - .actual_access:  read_only
        .address_space:  global
        .offset:         8
        .size:           8
        .value_kind:     global_buffer
      - .actual_access:  read_only
        .address_space:  global
        .offset:         16
        .size:           8
        .value_kind:     global_buffer
      - .actual_access:  read_only
        .address_space:  global
        .offset:         24
        .size:           8
        .value_kind:     global_buffer
      - .actual_access:  read_only
        .address_space:  global
        .offset:         32
        .size:           8
        .value_kind:     global_buffer
      - .actual_access:  write_only
        .address_space:  global
        .offset:         40
        .size:           8
        .value_kind:     global_buffer
    .group_segment_fixed_size: 128
    .kernarg_segment_align: 8
    .kernarg_segment_size: 48
    .language:       OpenCL C
    .language_version:
      - 2
      - 0
    .max_flat_workgroup_size: 256
    .name:           _Z9k3_gatherPKfS0_PKdPKiS2_Pf
    .private_segment_fixed_size: 0
    .sgpr_count:     30
    .sgpr_spill_count: 0
    .symbol:         _Z9k3_gatherPKfS0_PKdPKiS2_Pf.kd
    .uniform_work_group_size: 1
    .uses_dynamic_stack: false
    .vgpr_count:     24
    .vgpr_spill_count: 0
    .wavefront_size: 64
